# attention: window-branch first tile DMAs issued before the selected-branch accumulate; store-drain waits before two LDS-stage barriers removed
# speedup vs baseline: 1.0057x; 1.0017x over previous
; #define LDS_WAIT() asm volatile("s_waitcnt lgkmcnt(0)" ::: "memory")
; __device__ __forceinline__ unsigned f2bf(float f) { unsigned u = __builtin_bit_cast(unsigned, f); return (u + 0x7fffu + ((u >> 16) & 1u)) >> 16; }
; template <int BR>
; __device__ __forceinline__ void accum_branch(float* acc_g, bf16_t* out_g, const f32x16 (&o)[4], float fac, LAS float* li_l, int r32, int hi, unsigned* rmax = nullptr) {
;     if (hi == 0) li_l[r32] = fac;
;     LDS_WAIT();
;     float ld[4][4][4];
;     if (BR > 0) {
; #pragma unroll
;         for (int rr = 0; rr < 4; ++rr)
; #pragma unroll
;             for (int rq = 0; rq < 4; ++rq)
; #pragma unroll
;                 for (int d = 0; d < 4; ++d) ld[rr][rq][d] = (acc_g + (size_t)(rr + 4 * hi) * 2048 + r32)[rq * 128 + 32 * d]; }
;     __builtin_amdgcn_sched_barrier(0);
; #pragma unroll
;     for (int rr = 0; rr < 4; ++rr) {
;         float* ab = acc_g + (size_t)(rr + 4 * hi) * 2048 + r32; bf16_t* ob = out_g + (size_t)(rr + 4 * hi) * 2048 + r32;
;         float v[4][4];
; #pragma unroll
;         for (int rq = 0; rq < 4; ++rq) { const float f = li_l[rr + 8 * rq + 4 * hi];
; #pragma unroll
;             for (int d = 0; d < 4; ++d) { v[rq][d] = o[d][4 * rq + rr] * f; if (BR > 0) v[rq][d] += ld[rr][rq][d]; } }
;         float amx = 0.f;
; #pragma unroll
;         for (int rq = 0; rq < 4; ++rq)
; #pragma unroll
;             for (int d = 0; d < 4; ++d) { if (BR < 2) ab[rq * 128 + 32 * d] = v[rq][d]; else { const unsigned hb = f2bf(v[rq][d]); ob[rq * 128 + 32 * d] = (bf16_t)hb; amx = fmaxf(amx, fabsf(bflo(hb))); } }
.LBB0_622:
	s_or_b64 exec, exec, s[2:3]
	v_readlane_b32 s2, v245, 54
	v_readlane_b32 s12, v245, 56
	v_readlane_b32 s3, v245, 55
	s_add_i32 s2, s2, s12
	s_ashr_i32 s3, s2, 31
	s_lshl_b64 s[6:7], s[2:3], 13
	v_readlane_b32 s10, v245, 14
	s_add_u32 s6, s10, s6
	v_readlane_b32 s10, v245, 15
	s_addc_u32 s7, s10, s7
	v_readlane_b32 s10, v245, 59
	s_lshl_b32 s10, s10, 2
	s_waitcnt lgkmcnt(0)
	s_add_u32 s6, s6, s10
	s_addc_u32 s7, s7, 0
	v_readlane_b32 s13, v245, 57
	v_lshl_add_u32 v167, v170, 4, v71
	ds_read2_b32 v[74:75], v167 offset1:8
	v_lshlrev_b32_e32 v2, 2, v163
	v_lshl_add_u64 v[68:69], s[6:7], 0, v[2:3]
	v_lshlrev_b32_e32 v140, 2, v170
	v_ashrrev_i32_e32 v141, 31, v140
	s_waitcnt lgkmcnt(0)
	v_mul_f32_e32 v2, v20, v74
	v_mul_f32_e32 v20, v36, v74
	v_mul_f32_e32 v36, v52, v74
	v_mul_f32_e32 v4, v4, v74
	v_mul_f32_e32 v24, v24, v75
	v_mul_f32_e32 v40, v40, v75
	v_mul_f32_e32 v52, v56, v75
	v_mul_f32_e32 v8, v8, v75
	ds_read2_b32 v[74:75], v167 offset0:16 offset1:24
	v_lshlrev_b64 v[72:73], 13, v[140:141]
	v_lshl_add_u64 v[144:145], v[68:69], 0, v[72:73]
	s_waitcnt lgkmcnt(0)
	v_mul_f32_e32 v28, v28, v74
	v_mul_f32_e32 v44, v44, v74
	v_mul_f32_e32 v56, v60, v74
	v_mul_f32_e32 v12, v12, v74
	v_mul_f32_e32 v32, v32, v75
	v_mul_f32_e32 v48, v48, v75
	v_mul_f32_e32 v60, v64, v75
	v_mul_f32_e32 v16, v16, v75
	global_store_dword v[144:145], v2, off
	global_store_dword v[144:145], v20, off offset:128
	global_store_dword v[144:145], v36, off offset:256
	global_store_dword v[144:145], v4, off offset:384
	global_store_dword v[144:145], v24, off offset:512
	global_store_dword v[144:145], v40, off offset:640
	global_store_dword v[144:145], v52, off offset:768
	global_store_dword v[144:145], v8, off offset:896
	global_store_dword v[144:145], v28, off offset:1024
	global_store_dword v[144:145], v44, off offset:1152
	global_store_dword v[144:145], v56, off offset:1280
	global_store_dword v[144:145], v12, off offset:1408
	global_store_dword v[144:145], v32, off offset:1536
	global_store_dword v[144:145], v48, off offset:1664
	global_store_dword v[144:145], v60, off offset:1792
	global_store_dword v[144:145], v16, off offset:1920
	ds_read2_b32 v[74:75], v167 offset0:1 offset1:9
	v_or_b32_e32 v142, 1, v140
	v_ashrrev_i32_e32 v143, 31, v142
	v_lshlrev_b64 v[72:73], 13, v[142:143]
	v_lshl_add_u64 v[146:147], v[68:69], 0, v[72:73]
	s_waitcnt lgkmcnt(0)
	v_mul_f32_e32 v16, v5, v74
	ds_read2_b32 v[4:5], v167 offset0:17 offset1:25
	v_mul_f32_e32 v2, v21, v74
	v_mul_f32_e32 v8, v37, v74
	v_mul_f32_e32 v12, v53, v74
	v_mul_f32_e32 v20, v25, v75
	v_mul_f32_e32 v21, v41, v75
	v_mul_f32_e32 v24, v57, v75
	v_mul_f32_e32 v9, v9, v75
	s_waitcnt lgkmcnt(0)
	v_mul_f32_e32 v25, v29, v4
	v_mul_f32_e32 v28, v45, v4
	v_mul_f32_e32 v29, v61, v4
	v_mul_f32_e32 v4, v13, v4
	v_mul_f32_e32 v13, v33, v5
	v_mul_f32_e32 v32, v49, v5
	v_mul_f32_e32 v33, v65, v5
	v_mul_f32_e32 v5, v17, v5
	global_store_dword v[146:147], v2, off
	global_store_dword v[146:147], v8, off offset:128
	global_store_dword v[146:147], v12, off offset:256
	global_store_dword v[146:147], v16, off offset:384
	global_store_dword v[146:147], v20, off offset:512
	global_store_dword v[146:147], v21, off offset:640
	global_store_dword v[146:147], v24, off offset:768
	global_store_dword v[146:147], v9, off offset:896
	global_store_dword v[146:147], v25, off offset:1024
	global_store_dword v[146:147], v28, off offset:1152
	global_store_dword v[146:147], v29, off offset:1280
	global_store_dword v[146:147], v4, off offset:1408
	global_store_dword v[146:147], v13, off offset:1536
	global_store_dword v[146:147], v32, off offset:1664
	global_store_dword v[146:147], v33, off offset:1792
	global_store_dword v[146:147], v5, off offset:1920
	ds_read2_b32 v[8:9], v167 offset0:2 offset1:10
	v_or_b32_e32 v138, 2, v140
	v_ashrrev_i32_e32 v139, 31, v138
	v_lshlrev_b64 v[4:5], 13, v[138:139]
	v_lshl_add_u64 v[148:149], v[68:69], 0, v[4:5]
	s_waitcnt lgkmcnt(0)
; #define LAS __attribute__((address_space(3)))
; #define VM_WAIT() asm volatile("s_waitcnt vmcnt(0)" ::: "memory")
; __device__ __forceinline__ unsigned f2bf(float f) { unsigned u = __builtin_bit_cast(unsigned, f); return (u + 0x7fffu + ((u >> 16) & 1u)) >> 16; }
; template <int BR>
; __device__ __forceinline__ void accum_branch(float* acc_g, bf16_t* out_g, const f32x16 (&o)[4], float fac, LAS float* li_l, int r32, int hi, unsigned* rmax = nullptr) {
;     ...
; #pragma unroll
;     for (int rr = 0; rr < 4; ++rr) {
;         float* ab = acc_g + (size_t)(rr + 4 * hi) * 2048 + r32; bf16_t* ob = out_g + (size_t)(rr + 4 * hi) * 2048 + r32;
;         float v[4][4];
; #pragma unroll
;         for (int rq = 0; rq < 4; ++rq) { const float f = li_l[rr + 8 * rq + 4 * hi];
; #pragma unroll
;             for (int d = 0; d < 4; ++d) { v[rq][d] = o[d][4 * rq + rr] * f; if (BR > 0) v[rq][d] += ld[rr][rq][d]; } }
;         float amx = 0.f;
; #pragma unroll
;         for (int rq = 0; rq < 4; ++rq)
; #pragma unroll
;             for (int d = 0; d < 4; ++d) { if (BR < 2) ab[rq * 128 + 32 * d] = v[rq][d]; else { const unsigned hb = f2bf(v[rq][d]); ob[rq * 128 + 32 * d] = (bf16_t)hb; amx = fmaxf(amx, fabsf(bflo(hb))); } }
; __device__ __forceinline__ void attn_unit(const Frame& F, unsigned char* ws, int g, int qt) {
;     ...
;       LAS char* K_lds = lds + L_K;
;       __syncthreads();
;       { int offK[2], offV[2]; dma_offsets(128, wid, lane, offK, offV); dma_tile(K_lds, kc, 0, offK, wid); }
;       VM_WAIT(); __syncthreads();
	v_mul_f32_e32 v2, v22, v8
	v_mul_f32_e32 v12, v38, v8
	v_mul_f32_e32 v13, v54, v8
	v_mul_f32_e32 v6, v6, v8
	v_mul_f32_e32 v16, v26, v9
	v_mul_f32_e32 v17, v42, v9
	v_mul_f32_e32 v20, v58, v9
	v_mul_f32_e32 v10, v10, v9
	ds_read2_b32 v[8:9], v167 offset0:18 offset1:26
	s_waitcnt lgkmcnt(0)
	v_mul_f32_e32 v21, v30, v8
	v_mul_f32_e32 v22, v46, v8
	v_mul_f32_e32 v24, v62, v8
	v_mul_f32_e32 v8, v14, v8
	v_mul_f32_e32 v14, v34, v9
	v_mul_f32_e32 v25, v50, v9
	v_mul_f32_e32 v26, v66, v9
	v_mul_f32_e32 v9, v18, v9
	global_store_dword v[148:149], v2, off
	global_store_dword v[148:149], v12, off offset:128
	global_store_dword v[148:149], v13, off offset:256
	global_store_dword v[148:149], v6, off offset:384
	global_store_dword v[148:149], v16, off offset:512
	global_store_dword v[148:149], v17, off offset:640
	global_store_dword v[148:149], v20, off offset:768
	global_store_dword v[148:149], v10, off offset:896
	global_store_dword v[148:149], v21, off offset:1024
	global_store_dword v[148:149], v22, off offset:1152
	global_store_dword v[148:149], v24, off offset:1280
	global_store_dword v[148:149], v8, off offset:1408
	global_store_dword v[148:149], v14, off offset:1536
	global_store_dword v[148:149], v25, off offset:1664
	global_store_dword v[148:149], v26, off offset:1792
	global_store_dword v[148:149], v9, off offset:1920
	ds_read2_b32 v[8:9], v167 offset0:3 offset1:11
	v_or_b32_e32 v136, 3, v140
	v_ashrrev_i32_e32 v137, 31, v136
	v_lshlrev_b64 v[4:5], 13, v[136:137]
	v_lshl_add_u64 v[150:151], v[68:69], 0, v[4:5]
	s_waitcnt lgkmcnt(0)
	v_mul_f32_e32 v2, v23, v8
	v_mul_f32_e32 v10, v39, v8
	v_mul_f32_e32 v12, v55, v8
	v_mul_f32_e32 v8, v7, v8
	ds_read2_b32 v[6:7], v167 offset0:19 offset1:27
	v_mul_f32_e32 v13, v27, v9
	v_mul_f32_e32 v14, v43, v9
	v_mul_f32_e32 v16, v59, v9
	v_mul_f32_e32 v9, v11, v9
	s_waitcnt lgkmcnt(0)
	v_mul_f32_e32 v11, v31, v6
	v_mul_f32_e32 v17, v47, v6
	v_mul_f32_e32 v18, v63, v6
	v_mul_f32_e32 v6, v15, v6
	v_mul_f32_e32 v15, v35, v7
	v_mul_f32_e32 v20, v51, v7
	v_mul_f32_e32 v21, v67, v7
	v_mul_f32_e32 v7, v19, v7
	global_store_dword v[150:151], v2, off
	global_store_dword v[150:151], v10, off offset:128
	global_store_dword v[150:151], v12, off offset:256
	global_store_dword v[150:151], v8, off offset:384
	global_store_dword v[150:151], v13, off offset:512
	global_store_dword v[150:151], v14, off offset:640
	global_store_dword v[150:151], v16, off offset:768
	global_store_dword v[150:151], v9, off offset:896
	global_store_dword v[150:151], v11, off offset:1024
	global_store_dword v[150:151], v17, off offset:1152
	global_store_dword v[150:151], v18, off offset:1280
	global_store_dword v[150:151], v6, off offset:1408
	global_store_dword v[150:151], v15, off offset:1536
	global_store_dword v[150:151], v20, off offset:1664
	global_store_dword v[150:151], v21, off offset:1792
	global_store_dword v[150:151], v7, off offset:1920
	s_lshl_b32 s6, s30, 1
	s_or_b32 s34, s6, 1
	v_lshl_add_u32 v42, s34, 2, v159
	v_add_u32_e32 v40, s12, v159
	v_lshlrev_b32_e32 v2, 3, v174
	s_lshl_b32 s35, s30, 11
	v_bitop3_b32 v5, v42, v173, 7 bitop3:0x6c
	v_lshl_or_b32 v4, v40, 7, v2
	v_lshlrev_b32_e32 v41, 3, v5
	s_add_i32 s90, s35, 0
	v_lshl_or_b32 v6, v42, 7, v41
	s_add_i32 s6, s90, 0xc000
	v_ashrrev_i32_e32 v5, 31, v4
	v_lshl_add_u64 v[4:5], v[4:5], 1, s[14:15]
	s_mov_b32 s72, s6
	s_mov_b32 m0, s6
	v_ashrrev_i32_e32 v7, 31, v6
	s_add_i32 s6, s90, 0xc400
	s_waitcnt lgkmcnt(0)
	s_barrier
	global_load_lds_dwordx4 v[4:5], off
	v_lshl_add_u64 v[4:5], v[6:7], 1, s[14:15]
	s_mov_b32 m0, s6
	v_writelane_b32 v245, s6, 60
	global_load_lds_dwordx4 v[4:5], off
	s_waitcnt vmcnt(0)
	s_mov_b64 s[10:11], -1
	s_cmp_gt_i32 s18, 0
	s_mul_i32 s6, s30, 0x1080
	s_waitcnt vmcnt(0) lgkmcnt(0)
	s_barrier
	s_cbranch_scc1 .LBB0_624
	s_mul_i32 s7, s30, 0x1080
	s_mov_b64 s[10:11], 0

; #define VM_WAIT() asm volatile("s_waitcnt vmcnt(0)" ::: "memory")
; #define BAR() do { asm volatile("" ::: "memory"); __builtin_amdgcn_s_barrier(); asm volatile("" ::: "memory"); } while (0)
; #define DMA(ti, slot) do { const int _b = __builtin_amdgcn_readfirstlane(list[ti]); int offK[2], offV[2]; dma_offsets(ldk, wid, lane, offK, offV); \
;         dma_tile(K_lds + (slot) * SHM, Kb, (size_t)_b * 64 * ldk, offK, wid); dma_tile(V_lds + (slot) * SHM, Vb, (size_t)_b * 64 * ldk, offV, wid); } while (0)
; template <int MODE> ...
;     ...
;     DMA(0, 0); if (n > 1) DMA(1, 1); if (n > 2) DMA(2, 2);
;     VM_WAIT(); __syncthreads();
;     if (half) BAR();
.LBB0_793:
	s_cmp_lt_i32 s31, 1
	s_cbranch_scc1 .Lwpf_end
	v_readlane_b32 s54, v245, 44
	s_add_u32 s18, s14, 0x1000
	v_ashrrev_i32_e32 v153, 31, v152
	v_mov_b32_e32 v208, s54
	ds_read_b32 v208, v208
	s_addc_u32 s54, s15, 0
	s_add_u32 s55, s14, 0x1400
	s_addc_u32 s98, s15, 0
	s_mov_b32 m0, s72
	s_waitcnt lgkmcnt(0)
	v_readfirstlane_b32 s99, v208
	s_mul_hi_i32 s16, s99, 0x1e8000
	s_mul_i32 s99, s99, 0x1e8000
	s_add_u32 s52, s18, s99
	s_addc_u32 s53, s54, s16
	v_lshl_add_u64 v[246:247], v[152:153], 1, s[52:53]
	v_ashrrev_i32_e32 v157, 31, v156
	global_load_lds_dwordx4 v[246:247], off
	v_lshl_add_u64 v[246:247], v[156:157], 1, s[52:53]
	v_readlane_b32 s52, v245, 60
	s_mov_b32 m0, s52
	s_add_u32 s52, s55, s99
	s_addc_u32 s53, s98, s16
	v_ashrrev_i32_e32 v155, 31, v154
	global_load_lds_dwordx4 v[246:247], off
	v_lshl_add_u64 v[246:247], v[154:155], 1, s[52:53]
	s_mov_b32 m0, s90
	v_ashrrev_i32_e32 v159, 31, v158
	s_add_i32 s19, s90, 0x400
	global_load_lds_dwordx4 v[246:247], off
	v_lshl_add_u64 v[246:247], v[158:159], 1, s[52:53]
	s_mov_b32 m0, s19
	global_load_lds_dwordx4 v[246:247], off
	s_cmp_eq_u32 s31, 1
	s_cbranch_scc1 .Lwpf_a
	s_add_i32 s99, 0, 0x21064
	v_mov_b32_e32 v208, s99
	ds_read_b32 v208, v208
	s_waitcnt lgkmcnt(0)
	v_readfirstlane_b32 s99, v208
	s_mul_hi_i32 s16, s99, 0x1e8000
	s_mul_i32 s99, s99, 0x1e8000
	s_add_u32 s52, s18, s99
	s_addc_u32 s53, s54, s16
	s_add_i32 m0, s90, 0x10000
	v_lshl_add_u64 v[246:247], v[152:153], 1, s[52:53]
	global_load_lds_dwordx4 v[246:247], off
	s_add_i32 m0, s90, 0x10400
	v_lshl_add_u64 v[246:247], v[156:157], 1, s[52:53]
	s_add_u32 s52, s55, s99
	s_addc_u32 s53, s98, s16
	global_load_lds_dwordx4 v[246:247], off
	v_lshl_add_u64 v[246:247], v[154:155], 1, s[52:53]
	s_add_i32 m0, s90, 0x4000
	s_nop 0
	global_load_lds_dwordx4 v[246:247], off
	v_lshl_add_u64 v[246:247], v[158:159], 1, s[52:53]
	s_add_i32 m0, s90, 0x4400
	s_nop 0
	global_load_lds_dwordx4 v[246:247], off
.Lwpf_a:
	s_cmp_lt_u32 s31, 3
	s_cbranch_scc1 .Lwpf_end
	v_readlane_b32 s99, v245, 45
	s_nop 1
	v_mov_b32_e32 v208, s99
	ds_read_b32 v208, v208
	s_waitcnt lgkmcnt(0)
	v_readfirstlane_b32 s99, v208
	s_mul_hi_i32 s16, s99, 0x1e8000
	s_mul_i32 s99, s99, 0x1e8000
	s_add_u32 s52, s18, s99
	s_addc_u32 s53, s54, s16
	s_add_i32 m0, s90, 0x14000
	v_lshl_add_u64 v[246:247], v[152:153], 1, s[52:53]
	global_load_lds_dwordx4 v[246:247], off
	s_add_i32 m0, s90, 0x14400
	v_lshl_add_u64 v[246:247], v[156:157], 1, s[52:53]
	s_add_u32 s52, s55, s99
	s_addc_u32 s53, s98, s16
	global_load_lds_dwordx4 v[246:247], off
	v_lshl_add_u64 v[246:247], v[154:155], 1, s[52:53]
	s_add_i32 m0, s90, 0x8000
	s_nop 0
	global_load_lds_dwordx4 v[246:247], off
	v_lshl_add_u64 v[246:247], v[158:159], 1, s[52:53]
	s_add_i32 m0, s90, 0x8400
	s_nop 0
	global_load_lds_dwordx4 v[246:247], off

; __device__ __forceinline__ unsigned f2bf(float f) { unsigned u = __builtin_bit_cast(unsigned, f); return (u + 0x7fffu + ((u >> 16) & 1u)) >> 16; }
; template <int BR>
; __device__ __forceinline__ void accum_branch(float* acc_g, bf16_t* out_g, const f32x16 (&o)[4], float fac, LAS float* li_l, int r32, int hi, unsigned* rmax = nullptr) {
;     ...
;     float ld[4][4][4];
;     if (BR > 0) {
; #pragma unroll
;         for (int rr = 0; rr < 4; ++rr)
; #pragma unroll
;             for (int rq = 0; rq < 4; ++rq)
; #pragma unroll
;                 for (int d = 0; d < 4; ++d) ld[rr][rq][d] = (acc_g + (size_t)(rr + 4 * hi) * 2048 + r32)[rq * 128 + 32 * d]; }
;     __builtin_amdgcn_sched_barrier(0);
; #pragma unroll
;     for (int rr = 0; rr < 4; ++rr) {
;         float* ab = acc_g + (size_t)(rr + 4 * hi) * 2048 + r32; bf16_t* ob = out_g + (size_t)(rr + 4 * hi) * 2048 + r32;
;         float v[4][4];
; #pragma unroll
;         for (int rq = 0; rq < 4; ++rq) { const float f = li_l[rr + 8 * rq + 4 * hi];
; #pragma unroll
;             for (int d = 0; d < 4; ++d) { v[rq][d] = o[d][4 * rq + rr] * f; if (BR > 0) v[rq][d] += ld[rr][rq][d]; } }
;         float amx = 0.f;
; #pragma unroll
;         for (int rq = 0; rq < 4; ++rq)
; #pragma unroll
;             for (int d = 0; d < 4; ++d) { if (BR < 2) ab[rq * 128 + 32 * d] = v[rq][d]; else { const unsigned hb = f2bf(v[rq][d]); ob[rq * 128 + 32 * d] = (bf16_t)hb; amx = fmaxf(amx, fabsf(bflo(hb))); } }
.LBB0_795:
	s_or_b64 exec, exec, s[2:3]
	s_waitcnt lgkmcnt(0)
	global_load_dword v2, v[144:145], off
	global_load_dword v70, v[144:145], off offset:128
	global_load_dword v71, v[144:145], off offset:256
	global_load_dword v72, v[144:145], off offset:384
	global_load_dword v73, v[144:145], off offset:512
	global_load_dword v74, v[144:145], off offset:640
	global_load_dword v75, v[144:145], off offset:768
	global_load_dword v76, v[144:145], off offset:896
	global_load_dword v77, v[144:145], off offset:1024
	global_load_dword v78, v[144:145], off offset:1152
	global_load_dword v79, v[144:145], off offset:1280
	global_load_dword v80, v[144:145], off offset:1408
	global_load_dword v81, v[144:145], off offset:1536
	global_load_dword v82, v[144:145], off offset:1664
	global_load_dword v83, v[144:145], off offset:1792
	global_load_dword v84, v[144:145], off offset:1920
	global_load_dword v85, v[146:147], off
	global_load_dword v86, v[146:147], off offset:128
	global_load_dword v87, v[146:147], off offset:256
	global_load_dword v88, v[146:147], off offset:384
	global_load_dword v89, v[146:147], off offset:512
	global_load_dword v90, v[146:147], off offset:640
	global_load_dword v91, v[146:147], off offset:768
	global_load_dword v92, v[146:147], off offset:896
	global_load_dword v93, v[146:147], off offset:1024
	global_load_dword v94, v[146:147], off offset:1152
	global_load_dword v95, v[146:147], off offset:1280
	global_load_dword v96, v[146:147], off offset:1408
	global_load_dword v97, v[146:147], off offset:1536
	global_load_dword v98, v[146:147], off offset:1664
	global_load_dword v99, v[146:147], off offset:1792
	global_load_dword v135, v[146:147], off offset:1920
	global_load_dword v153, v[148:149], off
	global_load_dword v155, v[148:149], off offset:128
	global_load_dword v157, v[148:149], off offset:256
	global_load_dword v159, v[148:149], off offset:384
	global_load_dword v171, v[148:149], off offset:512
	global_load_dword v172, v[148:149], off offset:640
	global_load_dword v173, v[148:149], off offset:768
	global_load_dword v174, v[148:149], off offset:896
	global_load_dword v175, v[148:149], off offset:1024
	global_load_dword v176, v[148:149], off offset:1152
	global_load_dword v177, v[148:149], off offset:1280
	global_load_dword v178, v[148:149], off offset:1408
	global_load_dword v179, v[148:149], off offset:1536
	global_load_dword v180, v[148:149], off offset:1664
	global_load_dword v181, v[148:149], off offset:1792
	global_load_dword v182, v[148:149], off offset:1920
	global_load_dword v183, v[150:151], off
	global_load_dword v184, v[150:151], off offset:128
	global_load_dword v185, v[150:151], off offset:256
	global_load_dword v186, v[150:151], off offset:384
	global_load_dword v187, v[150:151], off offset:512
	global_load_dword v188, v[150:151], off offset:640
	global_load_dword v189, v[150:151], off offset:768
	global_load_dword v190, v[150:151], off offset:896
	global_load_dword v191, v[150:151], off offset:1024
	global_load_dword v192, v[150:151], off offset:1152
	global_load_dword v193, v[150:151], off offset:1280
	global_load_dword v195, v[150:151], off offset:1408
	global_load_dword v196, v[150:151], off offset:1536
	global_load_dword v197, v[150:151], off offset:1664
	global_load_dword v198, v[150:151], off offset:1792
	global_load_dword v199, v[150:151], off offset:1920
	ds_read2_b32 v[68:69], v167 offset1:8
	s_waitcnt vmcnt(0) lgkmcnt(0)
	v_fmac_f32_e32 v2, v20, v68
	v_fmac_f32_e32 v70, v36, v68
	v_fmac_f32_e32 v71, v52, v68
	v_fmac_f32_e32 v72, v4, v68
	v_fmac_f32_e32 v73, v24, v69
	v_fmac_f32_e32 v74, v40, v69
	v_fmac_f32_e32 v75, v56, v69
	v_fmac_f32_e32 v76, v8, v69
	ds_read2_b32 v[68:69], v167 offset0:16 offset1:24
	s_waitcnt lgkmcnt(0)
	v_fmac_f32_e32 v77, v28, v68
	v_fmac_f32_e32 v78, v44, v68
	v_fmac_f32_e32 v79, v60, v68
	v_fmac_f32_e32 v80, v12, v68
	v_fmac_f32_e32 v81, v32, v69
	v_fmac_f32_e32 v82, v48, v69
	v_fmac_f32_e32 v83, v64, v69
	v_fmac_f32_e32 v84, v16, v69
	global_store_dword v[144:145], v2, off
	global_store_dword v[144:145], v70, off offset:128
	global_store_dword v[144:145], v71, off offset:256
	global_store_dword v[144:145], v72, off offset:384
	global_store_dword v[144:145], v73, off offset:512
	global_store_dword v[144:145], v74, off offset:640
	global_store_dword v[144:145], v75, off offset:768
	global_store_dword v[144:145], v76, off offset:896
	global_store_dword v[144:145], v77, off offset:1024
	global_store_dword v[144:145], v78, off offset:1152
	global_store_dword v[144:145], v79, off offset:1280
	global_store_dword v[144:145], v80, off offset:1408
	global_store_dword v[144:145], v81, off offset:1536
	global_store_dword v[144:145], v82, off offset:1664
	global_store_dword v[144:145], v83, off offset:1792
	global_store_dword v[144:145], v84, off offset:1920
	ds_read2_b32 v[68:69], v167 offset0:1 offset1:9
	s_waitcnt lgkmcnt(0)
	v_fmac_f32_e32 v88, v5, v68
	ds_read2_b32 v[4:5], v167 offset0:17 offset1:25
	v_fmac_f32_e32 v85, v21, v68
	v_fmac_f32_e32 v86, v37, v68
	v_fmac_f32_e32 v87, v53, v68
	v_fmac_f32_e32 v89, v25, v69
	v_fmac_f32_e32 v90, v41, v69
	v_fmac_f32_e32 v91, v57, v69
	v_fmac_f32_e32 v92, v9, v69
	s_waitcnt lgkmcnt(0)
; #define VM_WAIT() asm volatile("s_waitcnt vmcnt(0)" ::: "memory")
; __device__ __forceinline__ unsigned f2bf(float f) { unsigned u = __builtin_bit_cast(unsigned, f); return (u + 0x7fffu + ((u >> 16) & 1u)) >> 16; }
; #define BAR() do { asm volatile("" ::: "memory"); __builtin_amdgcn_s_barrier(); asm volatile("" ::: "memory"); } while (0)
; #define DMA(ti, slot) do { const int _b = __builtin_amdgcn_readfirstlane(list[ti]); int offK[2], offV[2]; dma_offsets(ldk, wid, lane, offK, offV); \
;         dma_tile(K_lds + (slot) * SHM, Kb, (size_t)_b * 64 * ldk, offK, wid); dma_tile(V_lds + (slot) * SHM, Vb, (size_t)_b * 64 * ldk, offV, wid); } while (0)
; template <int MODE> ...
;     ...
;     for (int d = 0; d < 4; ++d) o[d] = f32x16{};
;     m_reg = -1e30f; l_reg = 0.f;
;     if (n <= 0) return;
;     const float ks = (MODE == 0) ? 16.f : 1.f;
;     const int half = wid >> 2;
;     ...
;     DMA(0, 0); if (n > 1) DMA(1, 1); if (n > 2) DMA(2, 2);
;     VM_WAIT(); __syncthreads();
;     if (half) BAR();
; template <int BR>
; __device__ __forceinline__ void accum_branch(float* acc_g, bf16_t* out_g, const f32x16 (&o)[4], float fac, LAS float* li_l, int r32, int hi, unsigned* rmax = nullptr) {
;     ...
;     for (int rr = 0; rr < 4; ++rr) {
;         float* ab = acc_g + (size_t)(rr + 4 * hi) * 2048 + r32; bf16_t* ob = out_g + (size_t)(rr + 4 * hi) * 2048 + r32;
;         float v[4][4];
; #pragma unroll
;         for (int rq = 0; rq < 4; ++rq) { const float f = li_l[rr + 8 * rq + 4 * hi];
; #pragma unroll
;             for (int d = 0; d < 4; ++d) { v[rq][d] = o[d][4 * rq + rr] * f; if (BR > 0) v[rq][d] += ld[rr][rq][d]; } }
;         float amx = 0.f;
; #pragma unroll
;         for (int rq = 0; rq < 4; ++rq)
; #pragma unroll
;             for (int d = 0; d < 4; ++d) { if (BR < 2) ab[rq * 128 + 32 * d] = v[rq][d]; else { const unsigned hb = f2bf(v[rq][d]); ob[rq * 128 + 32 * d] = (bf16_t)hb; amx = fmaxf(amx, fabsf(bflo(hb))); } }
	v_fmac_f32_e32 v93, v29, v4
	v_fmac_f32_e32 v94, v45, v4
	v_fmac_f32_e32 v95, v61, v4
	v_fmac_f32_e32 v96, v13, v4
	v_fmac_f32_e32 v97, v33, v5
	v_fmac_f32_e32 v98, v49, v5
	v_fmac_f32_e32 v99, v65, v5
	v_fmac_f32_e32 v135, v17, v5
	global_store_dword v[146:147], v85, off
	global_store_dword v[146:147], v86, off offset:128
	global_store_dword v[146:147], v87, off offset:256
	global_store_dword v[146:147], v88, off offset:384
	global_store_dword v[146:147], v89, off offset:512
	global_store_dword v[146:147], v90, off offset:640
	global_store_dword v[146:147], v91, off offset:768
	global_store_dword v[146:147], v92, off offset:896
	global_store_dword v[146:147], v93, off offset:1024
	global_store_dword v[146:147], v94, off offset:1152
	global_store_dword v[146:147], v95, off offset:1280
	global_store_dword v[146:147], v96, off offset:1408
	global_store_dword v[146:147], v97, off offset:1536
	global_store_dword v[146:147], v98, off offset:1664
	global_store_dword v[146:147], v99, off offset:1792
	global_store_dword v[146:147], v135, off offset:1920
	ds_read2_b32 v[4:5], v167 offset0:2 offset1:10
	s_waitcnt lgkmcnt(0)
	v_fmac_f32_e32 v153, v22, v4
	v_fmac_f32_e32 v155, v38, v4
	v_fmac_f32_e32 v157, v54, v4
	v_fmac_f32_e32 v159, v6, v4
	v_fmac_f32_e32 v171, v26, v5
	v_fmac_f32_e32 v172, v42, v5
	v_fmac_f32_e32 v173, v58, v5
	v_fmac_f32_e32 v174, v10, v5
	ds_read2_b32 v[4:5], v167 offset0:18 offset1:26
	s_waitcnt lgkmcnt(0)
	v_fmac_f32_e32 v179, v34, v5
	v_fmac_f32_e32 v175, v30, v4
	v_fmac_f32_e32 v176, v46, v4
	v_fmac_f32_e32 v177, v62, v4
	v_fmac_f32_e32 v178, v14, v4
	v_fmac_f32_e32 v180, v50, v5
	v_fmac_f32_e32 v181, v66, v5
	v_fmac_f32_e32 v182, v18, v5
	global_store_dword v[148:149], v153, off
	global_store_dword v[148:149], v155, off offset:128
	global_store_dword v[148:149], v157, off offset:256
	global_store_dword v[148:149], v159, off offset:384
	global_store_dword v[148:149], v171, off offset:512
	global_store_dword v[148:149], v172, off offset:640
	global_store_dword v[148:149], v173, off offset:768
	global_store_dword v[148:149], v174, off offset:896
	global_store_dword v[148:149], v175, off offset:1024
	global_store_dword v[148:149], v176, off offset:1152
	global_store_dword v[148:149], v177, off offset:1280
	global_store_dword v[148:149], v178, off offset:1408
	global_store_dword v[148:149], v179, off offset:1536
	global_store_dword v[148:149], v180, off offset:1664
	global_store_dword v[148:149], v181, off offset:1792
	global_store_dword v[148:149], v182, off offset:1920
	ds_read2_b32 v[4:5], v167 offset0:3 offset1:11
	s_waitcnt lgkmcnt(0)
	v_fmac_f32_e32 v183, v23, v4
	v_fmac_f32_e32 v184, v39, v4
	v_fmac_f32_e32 v185, v55, v4
	v_fmac_f32_e32 v186, v7, v4
	v_fmac_f32_e32 v187, v27, v5
	v_fmac_f32_e32 v188, v43, v5
	v_fmac_f32_e32 v189, v59, v5
	v_fmac_f32_e32 v190, v11, v5
	ds_read2_b32 v[4:5], v167 offset0:19 offset1:27
	s_waitcnt lgkmcnt(0)
	v_fmac_f32_e32 v191, v31, v4
	v_fmac_f32_e32 v192, v47, v4
	v_fmac_f32_e32 v193, v63, v4
	v_fmac_f32_e32 v195, v15, v4
	v_fmac_f32_e32 v196, v35, v5
	v_fmac_f32_e32 v197, v51, v5
	v_fmac_f32_e32 v198, v67, v5
	v_fmac_f32_e32 v199, v19, v5
	global_store_dword v[150:151], v183, off
	global_store_dword v[150:151], v184, off offset:128
	global_store_dword v[150:151], v185, off offset:256
	global_store_dword v[150:151], v186, off offset:384
	global_store_dword v[150:151], v187, off offset:512
	global_store_dword v[150:151], v188, off offset:640
	global_store_dword v[150:151], v189, off offset:768
	global_store_dword v[150:151], v190, off offset:896
	global_store_dword v[150:151], v191, off offset:1024
	global_store_dword v[150:151], v192, off offset:1152
	global_store_dword v[150:151], v193, off offset:1280
	global_store_dword v[150:151], v195, off offset:1408
	global_store_dword v[150:151], v196, off offset:1536
	global_store_dword v[150:151], v197, off offset:1664
	global_store_dword v[150:151], v198, off offset:1792
	global_store_dword v[150:151], v199, off offset:1920
	s_waitcnt lgkmcnt(0)
	v_mov_b32_e32 v19, 0
	s_cmp_lt_i32 s31, 1
	v_mov_b32_e32 v18, 0
	v_mov_b32_e32 v17, 0
	v_mov_b32_e32 v16, 0
	v_mov_b32_e32 v15, 0
	v_mov_b32_e32 v14, 0
	v_mov_b32_e32 v13, 0
	v_mov_b32_e32 v12, 0
	v_mov_b32_e32 v11, 0
	v_mov_b32_e32 v10, 0
	v_mov_b32_e32 v9, 0
	v_mov_b32_e32 v8, 0
	v_mov_b32_e32 v7, 0
	v_mov_b32_e32 v6, 0
	v_mov_b32_e32 v5, 0
	v_mov_b32_e32 v4, 0
	v_mov_b32_e32 v67, 0
	v_mov_b32_e32 v66, 0
	v_mov_b32_e32 v65, 0
	v_mov_b32_e32 v64, 0
	v_mov_b32_e32 v63, 0
	v_mov_b32_e32 v62, 0
	v_mov_b32_e32 v61, 0
	v_mov_b32_e32 v60, 0
	v_mov_b32_e32 v59, 0
	v_mov_b32_e32 v58, 0
	v_mov_b32_e32 v57, 0
	v_mov_b32_e32 v56, 0
	v_mov_b32_e32 v55, 0
	v_mov_b32_e32 v54, 0
	v_mov_b32_e32 v53, 0
	v_mov_b32_e32 v52, 0
	v_mov_b32_e32 v51, 0
	v_mov_b32_e32 v50, 0
	v_mov_b32_e32 v49, 0
	v_mov_b32_e32 v48, 0
	v_mov_b32_e32 v47, 0
	v_mov_b32_e32 v46, 0
	v_mov_b32_e32 v45, 0
	v_mov_b32_e32 v44, 0
	v_mov_b32_e32 v43, 0
	v_mov_b32_e32 v42, 0
	v_mov_b32_e32 v41, 0
	v_mov_b32_e32 v40, 0
	v_mov_b32_e32 v39, 0
	v_mov_b32_e32 v38, 0
	v_mov_b32_e32 v37, 0
	v_mov_b32_e32 v36, 0
	v_mov_b32_e32 v35, 0
	v_mov_b32_e32 v34, 0
	v_mov_b32_e32 v33, 0
	v_mov_b32_e32 v32, 0
	v_mov_b32_e32 v31, 0
	v_mov_b32_e32 v30, 0
	v_mov_b32_e32 v29, 0
	v_mov_b32_e32 v28, 0
	v_mov_b32_e32 v27, 0
	v_mov_b32_e32 v26, 0
	v_mov_b32_e32 v25, 0
	v_mov_b32_e32 v24, 0
	v_mov_b32_e32 v23, 0
	v_mov_b32_e32 v22, 0
	v_mov_b32_e32 v21, 0
	v_mov_b32_e32 v20, 0
	v_mov_b32_e32 v179, 0
	s_cbranch_scc1 .LBB0_852
	s_add_u32 s94, s14, 0x1000
	s_addc_u32 s2, s15, 0
	s_add_u32 s3, s14, 0x1400
	s_addc_u32 s6, s15, 0
	v_ashrrev_i32_e32 v153, 31, v152
	v_ashrrev_i32_e32 v157, 31, v156
	v_ashrrev_i32_e32 v155, 31, v154
	v_ashrrev_i32_e32 v159, 31, v158
	s_add_i32 s17, s90, 0x400
	s_mov_b32 s12, 0
	s_mov_b32 s13, 0x41800000
	s_cmp_lg_u32 s31, 1
	s_cselect_b64 s[64:65], -1, 0
.LBB0_800:
	s_cmp_lt_u32 s30, 4
	s_cselect_b64 s[8:9], -1, 0
	v_writelane_b32 v244, s8, 1
	s_and_b64 vcc, exec, s[8:9]
	s_waitcnt lgkmcnt(0)
	s_barrier
	v_writelane_b32 v244, s9, 2
	s_cbranch_vccnz .LBB0_802
	s_barrier
